# speedup vs baseline: 1.0114x; 1.0114x over previous
_Z11scan_kernelILi1ELi1536ELi4EEvPKfPKDF16_S3_S1_S1_PDv2_DF16_S3_Pf:
	s_cmpk_gt_i32 s2, 0x5ff
	s_cbranch_scc1 .LBB2_15
	s_cmpk_gt_i32 s2, 0x3ff
	s_cbranch_scc1 .Lstag_done_p1
	s_getreg_b32 s20, hwreg(HW_REG_HW_ID, 0, 2)
	s_cmp_eq_u32 s20, 0
	s_cbranch_scc1 .Lstag_done_p1
.Lstag_loop_p1:
	s_sleep 40
	s_add_i32 s20, s20, -1
	s_cmp_lg_u32 s20, 0
	s_cbranch_scc1 .Lstag_loop_p1
.Lstag_done_p1:
	s_ashr_i32 s15, s2, 3
	s_mul_hi_i32 s14, s15, 0x55555556
	s_lshr_b32 s12, s14, 31
	s_add_i32 s14, s14, s12
	s_mul_i32 s16, s14, 0x3fffffd
	s_add_i32 s16, s16, s15
	s_lshl_b32 s15, s16, 6
	s_lshl_b32 s16, s2, 5
	s_and_b32 s16, s16, 32
	s_or_b32 s15, s15, s16
	s_bfe_u32 s16, s2, 0x20001
	s_mul_i32 s2, s16, 0xc0
	s_lshl_b32 s12, s14, 1
	s_add_i32 s17, s15, s2
	s_load_dwordx8 s[4:11], s[0:1], 0x0
	s_and_b32 s12, s12, -16
	s_lshl_b32 s13, s14, 4
	s_and_b32 s13, s13, 0x70
	s_mov_b32 s3, 0
	v_mov_b32_e32 v32, 0
	v_lshrrev_b32_e32 v78, 6, v0
	v_bfe_u32 v65, v0, 2, 4
	v_lshlrev_b32_e32 v1, 4, v0
	v_and_b32_e32 v30, 48, v1
	v_lshl_add_u32 v1, v78, 7, v65
	v_lshl_add_u32 v1, v1, 9, v30
	s_lshl_b32 s18, s17, 7
	s_add_i32 s18, s18, s12
	s_lshl_b32 s18, s18, 9
	s_lshl_b32 s2, s13, 2
	s_add_i32 s18, s18, s2
	s_waitcnt lgkmcnt(0)
	s_add_u32 s20, s4, s18
	s_addc_u32 s21, s5, 0
	s_add_u32 s22, s20, 0x40000
	s_addc_u32 s23, s21, 0
	s_add_u32 s24, s22, 0x40000
	s_addc_u32 s25, s23, 0
	s_add_u32 s26, s24, 0x40000
	s_addc_u32 s27, s25, 0
	s_add_u32 s28, s26, 0x40000
	s_addc_u32 s29, s27, 0
	s_add_u32 s30, s28, 0x40000
	s_addc_u32 s31, s29, 0
	s_add_u32 s32, s30, 0x40000
	s_addc_u32 s33, s31, 0
	s_add_u32 s34, s32, 0x40000
	s_addc_u32 s35, s33, 0
	global_load_dwordx4 v[2:5], v1, s[34:35]
	global_load_dwordx4 v[6:9], v1, s[32:33]
	global_load_dwordx4 v[10:13], v1, s[30:31]
	global_load_dwordx4 v[14:17], v1, s[28:29]
	global_load_dwordx4 v[18:21], v1, s[26:27]
	global_load_dwordx4 v[22:25], v1, s[24:25]
	v_bfe_u32 v103, v0, 5, 1
	v_lshrrev_b32_e32 v33, 2, v0
	global_load_dwordx4 v[66:69], v1, s[22:23]
	global_load_dwordx4 v[74:77], v1, s[20:21]
	v_lshlrev_b32_e32 v104, 1, v78
	v_and_b32_e32 v27, 3, v0
	v_lshrrev_b32_e32 v28, 1, v0
	v_and_or_b32 v59, v33, 1, v104
	v_and_or_b32 v105, v28, 12, v27
	v_lshlrev_b32_e32 v28, 4, v103
	v_mov_b32_e32 v29, v32
	v_lshl_add_u64 v[56:57], s[6:7], 0, v[28:29]
	v_or_b32_e32 v27, s13, v59
	v_or_b32_e32 v28, s12, v105
	s_lshl_b32 s4, s16, 16
	v_lshl_add_u32 v31, v27, 7, v28
	s_or_b32 s2, s4, 0x4000
	v_add_u32_e32 v27, 0x400, v31
	s_or_b32 s5, s4, 0xc000
	v_add_u32_e32 v28, s2, v27
	v_and_b32_e32 v1, 31, v0
	v_ashrrev_i32_e32 v29, 31, v28
	v_add_u32_e32 v34, s5, v27
	v_or_b32_e32 v26, s15, v1
	v_lshlrev_b64 v[28:29], 5, v[28:29]
	v_ashrrev_i32_e32 v35, 31, v34
	v_lshl_add_u64 v[28:29], v[56:57], 0, v[28:29]
	v_lshlrev_b64 v[34:35], 5, v[34:35]
	v_lshl_or_b32 v58, v26, 1, v103
	v_lshl_add_u64 v[34:35], v[56:57], 0, v[34:35]
	global_load_dwordx4 v[36:39], v[28:29], off
	global_load_dwordx4 v[40:43], v[34:35], off
	v_add_u32_e32 v28, 0x180, v58
	v_ashrrev_i32_e32 v29, 31, v28
	v_add_u32_e32 v34, 0x480, v58
	v_lshl_add_u64 v[28:29], v[28:29], 4, s[8:9]
	v_ashrrev_i32_e32 v35, 31, v34
	v_ashrrev_i32_e32 v27, 31, v26
	v_lshl_add_u64 v[34:35], v[34:35], 4, s[8:9]
	global_load_dwordx4 v[44:47], v[28:29], off
	global_load_dwordx4 v[48:51], v[34:35], off
	v_lshl_add_u64 v[60:61], v[26:27], 2, s[10:11]
	v_add_u32_e32 v26, s5, v31
	v_add_u32_e32 v28, s2, v31
	v_ashrrev_i32_e32 v27, 31, v26
	v_ashrrev_i32_e32 v29, 31, v28
	v_lshlrev_b64 v[26:27], 5, v[26:27]
	v_lshlrev_b64 v[28:29], 5, v[28:29]
	global_load_dword v62, v[60:61], off offset:768
	global_load_dword v64, v[60:61], off offset:2304
	v_lshl_add_u64 v[26:27], v[56:57], 0, v[26:27]
	v_lshl_add_u64 v[28:29], v[56:57], 0, v[28:29]
	global_load_dwordx4 v[52:55], v[26:27], off
	s_nop 0
	global_load_dwordx4 v[26:29], v[28:29], off
	s_load_dwordx2 s[0:1], s[0:1], 0x28
	v_and_b32_e32 v0, 63, v0
	v_bfrev_b32_e32 v31, 60
	v_cmp_gt_u32_e32 vcc, 32, v0
	v_mul_u32_u24_e32 v102, 0x410, v1
	v_lshlrev_b32_e32 v0, 2, v1
	v_mov_b32_e32 v1, v32
	v_cndmask_b32_e64 v34, v31, 0, vcc
	s_waitcnt lgkmcnt(0)
	v_lshl_add_u64 v[72:73], s[0:1], 0, v[0:1]
	v_mul_u32_u24_e32 v0, 0x410, v78
	v_lshlrev_b32_e32 v1, 6, v65
	v_add3_u32 v1, v0, v1, v30
	s_mul_i32 s16, s16, 24
	s_lshr_b32 s0, s15, 5
	s_waitcnt vmcnt(8)
	ds_write_b128 v1, v[74:77]
	ds_write_b128 v1, v[66:69] offset:4160
	ds_write_b128 v1, v[22:25] offset:8320
	ds_write_b128 v1, v[18:21] offset:12480
	ds_write_b128 v1, v[14:17] offset:16640
	ds_write_b128 v1, v[10:13] offset:20800
	ds_write_b128 v1, v[6:9] offset:24960
	ds_write_b128 v1, v[2:5] offset:29120
	s_add_i32 s0, s0, s16
	s_waitcnt lgkmcnt(0)
	s_barrier
	s_lshl_b32 s2, s0, 10
	v_mov_b32_e32 v33, v32
	v_mov_b32_e32 v35, v32
	v_lshl_or_b32 v106, v103, 2, v102
	s_add_i32 s5, s2, 0x4800
	v_or_b32_e32 v107, s13, v103
	s_ashr_i32 s6, s14, 3
	s_add_i32 s7, s2, 0x1800
	s_mov_b64 s[0:1], -1
	s_mov_b32 s10, 0x7f61b1e6
	s_mov_b32 s11, 0x42800000
	s_waitcnt vmcnt(3)
	v_mov_b32_e32 v63, v62
	s_waitcnt vmcnt(2)
	v_mov_b32_e32 v65, v64
	s_waitcnt vmcnt(0)
	s_branch .LBB2_3

.LBB2_15:
	s_endpgm
	.p2alignl 8, 3212836864

_Z11scan_kernelILi3ELi1536ELi3EEvPKfPKDF16_S3_S1_S1_PDv2_DF16_S3_Pf:
	s_cmpk_gt_i32 s2, 0x5ff
	s_cbranch_scc1 .LBB3_20
	s_cmpk_gt_i32 s2, 0x2ff
	s_cbranch_scc1 .Lstag_done_p3
	s_getreg_b32 s20, hwreg(HW_REG_HW_ID, 0, 2)
	s_cmp_eq_u32 s20, 0
	s_cbranch_scc1 .Lstag_done_p3

.Lstag_done_p3:
	s_load_dwordx8 s[4:11], s[0:1], 0x0
	s_load_dwordx2 s[16:17], s[0:1], 0x20
	s_load_dwordx4 s[12:15], s[0:1], 0x30
	s_ashr_i32 s0, s2, 3
	s_mul_hi_i32 s18, s0, 0x55555556
	s_lshr_b32 s19, s18, 31
	s_add_i32 s21, s18, s19
	s_mul_i32 s18, s21, 0x3fffffd
	s_bfe_u32 s1, s2, 0x20001
	s_add_i32 s18, s18, s0
	s_lshl_b32 s2, s2, 5
	s_lshl_b32 s0, s18, 6
	s_and_b32 s2, s2, 32
	s_or_b32 s0, s0, s2
	s_lshl_b32 s2, s21, 1
	s_and_b32 s19, s2, -16
	s_lshl_b32 s2, s21, 4
	s_and_b32 s20, s2, 0x70
	s_mul_i32 s2, s1, 0xc0
	s_add_i32 s18, s0, s2
	s_mov_b32 s3, 0
	v_mov_b32_e32 v50, 0
	v_lshrrev_b32_e32 v142, 6, v0
	v_bfe_u32 v45, v0, 2, 4
	v_lshlrev_b32_e32 v1, 4, v0
	v_and_b32_e32 v34, 48, v1
	v_lshl_add_u32 v1, v142, 7, v45
	v_lshl_add_u32 v1, v1, 9, v34
	s_lshl_b32 s22, s18, 7
	s_add_i32 s22, s22, s19
	s_lshl_b32 s22, s22, 9
	s_lshl_b32 s2, s20, 2
	s_add_i32 s22, s22, s2
	s_waitcnt lgkmcnt(0)
	s_add_u32 s24, s4, s22
	s_addc_u32 s25, s5, 0
	s_add_u32 s26, s24, 0x40000
	s_addc_u32 s27, s25, 0
	s_add_u32 s28, s26, 0x40000
	s_addc_u32 s29, s27, 0
	s_add_u32 s30, s28, 0x40000
	s_addc_u32 s31, s29, 0
	s_add_u32 s32, s30, 0x40000
	s_addc_u32 s33, s31, 0
	s_add_u32 s34, s32, 0x40000
	s_addc_u32 s35, s33, 0
	s_add_u32 s36, s34, 0x40000
	s_addc_u32 s37, s35, 0
	s_add_u32 s38, s36, 0x40000
	s_addc_u32 s39, s37, 0
	global_load_dwordx4 v[2:5], v1, s[38:39]
	global_load_dwordx4 v[6:9], v1, s[36:37]
	global_load_dwordx4 v[10:13], v1, s[34:35]
	global_load_dwordx4 v[14:17], v1, s[32:33]
	global_load_dwordx4 v[18:21], v1, s[30:31]
	global_load_dwordx4 v[22:25], v1, s[28:29]
	v_and_b32_e32 v35, 31, v0
	global_load_dwordx4 v[26:29], v1, s[26:27]
	global_load_dwordx4 v[30:33], v1, s[24:25]
	v_or_b32_e32 v36, s0, v35
	v_ashrrev_i32_e32 v37, 31, v36
	v_lshlrev_b64 v[38:39], 2, v[36:37]
	v_lshlrev_b32_e32 v89, 1, v142
	v_and_b32_e32 v1, 3, v0
	v_lshrrev_b32_e32 v37, 1, v0
	v_lshl_add_u64 v[40:41], s[16:17], 0, v[38:39]
	v_and_or_b32 v144, v37, 12, v1
	v_or_b32_e32 v1, s20, v89
	global_load_dword v94, v[40:41], off
	v_bfe_u32 v143, v0, 2, 1
	v_lshlrev_b32_e32 v40, 1, v35
	v_mov_b32_e32 v41, v50
	v_or_b32_e32 v37, 8, v1
	v_bfe_u32 v95, v0, 5, 1
	s_lshl_b32 s4, s1, 16
	v_lshl_add_u64 v[86:87], s[12:13], 0, v[40:41]
	v_or_b32_e32 v51, s19, v144
	v_or_b32_e32 v40, v37, v143
	v_lshlrev_b32_e32 v82, 4, v95
	v_mov_b32_e32 v83, v50
	s_ashr_i32 s5, s0, 5
	s_or_b32 s0, s4, 0x4000
	v_lshl_add_u32 v42, v40, 7, v51
	v_lshl_add_u64 v[84:85], s[6:7], 0, v[82:83]
	s_or_b32 s2, s4, 0xc000
	s_mul_i32 s7, s1, 24
	v_add_u32_e32 v40, s0, v42
	s_or_b32 s1, s7, 6
	v_ashrrev_i32_e32 v41, 31, v40
	v_add_u32_e32 v42, s2, v42
	s_add_i32 s6, s5, 12
	s_ashr_i32 s12, s21, 3
	s_add_i32 s13, s1, s5
	v_lshlrev_b64 v[40:41], 5, v[40:41]
	v_ashrrev_i32_e32 v43, 31, v42
	v_or_b32_e32 v37, v37, v95
	s_lshl_b32 s13, s13, 10
	s_add_i32 s1, s1, s6
	v_lshl_add_u64 v[40:41], v[84:85], 0, v[40:41]
	v_lshlrev_b64 v[42:43], 5, v[42:43]
	v_lshl_add_u32 v37, v37, 3, s12
	s_lshl_b32 s1, s1, 10
	v_lshl_add_u64 v[42:43], v[84:85], 0, v[42:43]
	global_load_dwordx4 v[58:61], v[40:41], off
	global_load_dwordx4 v[62:65], v[42:43], off
	v_add_u32_e32 v40, s13, v37
	v_ashrrev_i32_e32 v41, 31, v40
	v_add_u32_e32 v42, s1, v37
	v_lshlrev_b64 v[40:41], 6, v[40:41]
	v_ashrrev_i32_e32 v43, 31, v42
	v_lshl_or_b32 v88, v36, 1, v95
	v_lshl_add_u64 v[40:41], v[86:87], 0, v[40:41]
	v_lshlrev_b64 v[42:43], 6, v[42:43]
	v_add_u32_e32 v36, 0x180, v88
	v_lshl_add_u64 v[42:43], v[86:87], 0, v[42:43]
	global_load_ushort v145, v[40:41], off
	global_load_ushort v146, v[42:43], off
	v_ashrrev_i32_e32 v37, 31, v36
	v_add_u32_e32 v40, 0x480, v88
	v_lshl_add_u64 v[36:37], v[36:37], 4, s[8:9]
	v_ashrrev_i32_e32 v41, 31, v40
	v_lshl_add_u64 v[40:41], v[40:41], 4, s[8:9]
	global_load_dwordx4 v[66:69], v[36:37], off
	global_load_dwordx4 v[70:73], v[40:41], off
	v_or_b32_e32 v36, v1, v95
	v_lshl_add_u64 v[90:91], s[10:11], 0, v[38:39]
	v_lshl_add_u32 v38, v36, 3, s12
	v_add_u32_e32 v36, s1, v38
	v_ashrrev_i32_e32 v37, 31, v36
	v_add_u32_e32 v38, s13, v38
	v_lshlrev_b64 v[36:37], 6, v[36:37]
	v_ashrrev_i32_e32 v39, 31, v38
	v_or_b32_e32 v1, v1, v143
	v_lshl_add_u64 v[36:37], v[86:87], 0, v[36:37]
	v_lshlrev_b64 v[38:39], 6, v[38:39]
	v_lshl_add_u32 v1, v1, 7, v51
	global_load_dword v92, v[90:91], off offset:2304
	global_load_dword v96, v[90:91], off offset:768
	v_lshl_add_u64 v[38:39], v[86:87], 0, v[38:39]
	global_load_ushort v150, v[36:37], off
	global_load_ushort v151, v[38:39], off
	v_add_u32_e32 v36, s2, v1
	v_ashrrev_i32_e32 v37, 31, v36
	v_add_u32_e32 v38, s0, v1
	v_lshlrev_b64 v[36:37], 5, v[36:37]
	v_ashrrev_i32_e32 v39, 31, v38
	v_lshl_add_u64 v[36:37], v[84:85], 0, v[36:37]
	v_lshlrev_b64 v[38:39], 5, v[38:39]
	v_lshl_add_u64 v[38:39], v[84:85], 0, v[38:39]
	global_load_dwordx4 v[74:77], v[36:37], off
	global_load_dwordx4 v[78:81], v[38:39], off
	v_and_b32_e32 v1, 63, v0
	v_cmp_gt_u32_e32 vcc, 32, v1
	v_bfrev_b32_e32 v1, 60
	v_mul_u32_u24_e32 v83, 0x210, v35
	v_mov_b32_e32 v36, 0x3c00
	v_cndmask_b32_e64 v56, v1, 0, vcc
	v_mul_u32_u24_e32 v1, 0x410, v35
	v_lshl_or_b32 v35, v95, 1, v83
	v_cndmask_b32_e64 v53, v36, 0, vcc
	v_add_u32_e32 v148, 0x8200, v35
	v_mul_u32_u24_e32 v35, 0x410, v142
	v_lshlrev_b32_e32 v36, 6, v45
	v_add3_u32 v34, v35, v36, v34
	s_waitcnt vmcnt(13)
	ds_write_b128 v34, v[30:33]
	ds_write_b128 v34, v[26:29] offset:4160
	ds_write_b128 v34, v[22:25] offset:8320
	ds_write_b128 v34, v[18:21] offset:12480
	ds_write_b128 v34, v[14:17] offset:16640
	ds_write_b128 v34, v[10:13] offset:20800
	ds_write_b128 v34, v[6:9] offset:24960
	ds_write_b128 v34, v[2:5] offset:29120
	s_waitcnt lgkmcnt(0)
	s_barrier
	v_mov_b32_e32 v51, v50
	v_mov_b32_e32 v52, v50
	v_mov_b32_e32 v54, v50
	v_mov_b32_e32 v55, v50
	v_mov_b32_e32 v57, v50
	v_lshl_or_b32 v147, v95, 2, v1
	s_mov_b64 s[0:1], -1
	s_mov_b32 s10, 0x7f61b1e6
	s_mov_b32 s11, 0x42800000
	s_waitcnt vmcnt(5)
	v_mov_b32_e32 v93, v92
	s_waitcnt vmcnt(4)
	v_mov_b32_e32 v97, v96
	s_branch .LBB3_3

.LBB3_19:
	s_waitcnt lgkmcnt(0)
	s_barrier
	s_lshl_b32 s0, s20, 2
	s_add_u32 s0, s14, s0
	s_addc_u32 s1, s15, 0
	s_lshl_b32 s2, s18, 7
	s_add_i32 s2, s2, s19
	s_lshl_b32 s2, s2, 9
	s_add_u32 s24, s0, s2
	s_addc_u32 s25, s1, 0
	s_add_u32 s26, s24, 0x40000
	s_addc_u32 s27, s25, 0
	s_add_u32 s28, s26, 0x40000
	s_addc_u32 s29, s27, 0
	s_add_u32 s30, s28, 0x40000
	s_addc_u32 s31, s29, 0
	s_add_u32 s32, s30, 0x40000
	s_addc_u32 s33, s31, 0
	s_add_u32 s34, s32, 0x40000
	s_addc_u32 s35, s33, 0
	s_add_u32 s36, s34, 0x40000
	s_addc_u32 s37, s35, 0
	s_add_u32 s38, s36, 0x40000
	s_addc_u32 s39, s37, 0
	v_lshrrev_b32_e32 v1, 6, v0
	v_bfe_u32 v36, v0, 2, 4
	v_lshlrev_b32_e32 v37, 4, v0
	v_and_b32_e32 v37, 48, v37
	v_lshl_add_u32 v10, v1, 7, v36
	v_lshl_add_u32 v10, v10, 9, v37
	v_mul_u32_u24_e32 v1, 0x410, v1
	v_lshl_add_u32 v36, v36, 6, v37
	v_add_u32_e32 v11, v1, v36
	ds_read_b128 v[2:5], v11
	ds_read_b128 v[6:9], v11 offset:4160
	ds_read_b128 v[12:15], v11 offset:8320
	ds_read_b128 v[16:19], v11 offset:12480
	ds_read_b128 v[20:23], v11 offset:16640
	ds_read_b128 v[24:27], v11 offset:20800
	ds_read_b128 v[28:31], v11 offset:24960
	ds_read_b128 v[32:35], v11 offset:29120
	s_waitcnt lgkmcnt(7)
	global_store_dwordx4 v10, v[2:5], s[24:25] nt
	s_waitcnt lgkmcnt(6)
	global_store_dwordx4 v10, v[6:9], s[26:27] nt
	s_waitcnt lgkmcnt(5)
	global_store_dwordx4 v10, v[12:15], s[28:29] nt
	s_waitcnt lgkmcnt(4)
	global_store_dwordx4 v10, v[16:19], s[30:31] nt
	s_waitcnt lgkmcnt(3)
	global_store_dwordx4 v10, v[20:23], s[32:33] nt
	s_waitcnt lgkmcnt(2)
	global_store_dwordx4 v10, v[24:27], s[34:35] nt
	s_waitcnt lgkmcnt(1)
	global_store_dwordx4 v10, v[28:31], s[36:37] nt
	s_waitcnt lgkmcnt(0)
	global_store_dwordx4 v10, v[32:35], s[38:39] nt

	.text
	.p2alignl 6, 3212836864
	.fill 256, 4, 3212836864
	.p2alignl 8, 3212836864
